# v42 + hazard audit: the 4 dead wait states (s_nop 3) between the QK and PV sections of the waves 0-3 steady loop removed
# baseline (speedup 1.0000x reference)
; template <bool FOX>
; __device__ __forceinline__ void attn_unit(const Args& A, int b, int h, int qb, LAS char* shm, LAS float* dg) {
;     ...
;         if (t == 1 && 4 < nti) ISSUE_K(t0 + 4, 0);
;         if (t + 4 < nti) ISSUE_K(t0 + t + 4, t % NS);
;         if (t + 2 < nti) ISSUE_V(t0 + t + 2, (t + 2) % NS);
;         SFENCE();
;         { if constexpr (!FOX) { if (t0 + t == tw_last + 1) {
; #pragma unroll
;                   for (int r = 0; r < 16; ++r) negm[r] = -INFINITY;
;                   asm volatile("" : "+v"(negm)); } }
;           const lds_cptr vp = vp0 + ((t - 1) % NS) * VSLOT; float sa = 0.f, sb = 0.f;
; #pragma unroll
;           for (int g = 0; g < 2 * NQ; ++g) {
;               if (!FOX && g == 0) c0 = __builtin_amdgcn_mfma_f32_32x32x16_bf16(kf[0], qr[0], negm, 0, 0, 0);
;               else if (!FOX && g == 1) c1 = __builtin_amdgcn_mfma_f32_32x32x16_bf16(kf[1], qr[0], negm, 0, 0, 0);
;               else if (g & 1) c1 = __builtin_amdgcn_mfma_f32_32x32x16_bf16(kf[g], qr[g >> 1], c1, 0, 0, 0); else c0 = __builtin_amdgcn_mfma_f32_32x32x16_bf16(kf[g], qr[g >> 1], c0, 0, 0, 0);
;               if (g < 8) { const int i = (g >> 1) + 4 * (g & 1); vlo[i] = vtr(vp + (i >> 2) * 4096 + (i & 3) * 1024); vhi[i] = vtr(vp + (i >> 2) * 4096 + (i & 3) * 1024 + 512);
;                   if (g < 4) { sa += pp0[4 * g]; sb += pp0[4 * g + 1]; sa += pp0[4 * g + 2]; sb += pp0[4 * g + 3]; } else { sa += pp1[4 * g - 16]; sb += pp1[4 * g - 15]; sa += pp1[4 * g - 14]; sb += pp1[4 * g - 13]; }
;                   asm volatile("" : "+v"(sa), "+v"(sb)); }
;               { constexpr int G0 = FOX ? 0 : 4; if (g >= G0) { const int q = 2 * (g - G0);
; #pragma unroll
;                   for (int k = 0; k < 2; ++k) { const int w = q + k; const unsigned pkd = w < 8 ? cvt_pk_bf16(pp0[2 * w], pp0[2 * w + 1]) : cvt_pk_bf16(pp1[2 * w - 16], pp1[2 * w - 15]); pw[w >> 2][w & 3] = pkd; } } }
;               SFENCE();
;           }
;           lrun += sa + sb; }
;         MASKONLY(t);
;         float rm; ROWMAX(rm);
;         bool resc = false;
;         if (__any(rm > THR)) { const float dl = fmaxf(rm, 0.f); mhat += dl;
; #pragma unroll
;             for (int r = 0; r < 16; ++r) { c0[r] -= dl; c1[r] -= dl; }
;             if constexpr (!FOX) {
; #pragma unroll
;                 for (int r = 0; r < 16; ++r) negm[r] = -mhat;
;                 asm volatile("" : "+v"(negm)); }
.Lmla_ss1_in:
	s_mov_b32 m0, s52
	s_nop 0
	global_load_lds_dwordx4 v240, s[46:47]
	s_add_i32 m0, s52, 0x2000
	s_nop 0
	global_load_lds_dwordx4 v240, s[98:99]
	s_mov_b32 m0, s53
	s_nop 0
	global_load_lds_dwordx4 v240, s[60:61]
	s_waitcnt lgkmcnt(0)
	s_add_i32 s27, s42, 0x8000
	v_mfma_f32_32x32x16_bf16 v[114:129], v[206:209], v[138:141], v[82:97]
	s_and_b32 s27, s27, 0x6000
	s_add_u32 s42, s42, 0x2000
	s_addc_u32 s43, s43, 0
	v_add_u32_e32 v3, s27, v247
	ds_read_b64_tr_b16 v[206:207], v3 offset:49152
	ds_read_b64_tr_b16 v[208:209], v3 offset:49664
	v_add_f32_e32 v4, v69, v67
	v_add_f32_e32 v5, v68, v66
	v_mfma_f32_32x32x16_bf16 v[98:113], v[194:197], v[138:141], v[82:97]
	ds_read_b64_tr_b16 v[194:195], v3 offset:53248
	ds_read_b64_tr_b16 v[196:197], v3 offset:53760
	v_add_f32_e32 v4, v71, v4
	v_add_f32_e32 v5, v70, v5
	v_add_f32_e32 v4, v73, v4
	v_add_f32_e32 v5, v72, v5
	v_mfma_f32_32x32x16_bf16 v[114:129], v[202:205], v[142:145], v[114:129]
	ds_read_b64_tr_b16 v[202:203], v3 offset:50176
	ds_read_b64_tr_b16 v[204:205], v3 offset:50688
	v_add_f32_e32 v4, v75, v4
	v_add_f32_e32 v5, v74, v5
	v_add_f32_e32 v4, v77, v4
	v_add_f32_e32 v5, v76, v5
	v_mfma_f32_32x32x16_bf16 v[98:113], v[186:189], v[142:145], v[98:113]
	ds_read_b64_tr_b16 v[214:215], v3 offset:54272
	ds_read_b64_tr_b16 v[216:217], v3 offset:54784
	v_add_f32_e32 v4, v79, v4
	v_add_f32_e32 v5, v78, v5
	v_add_f32_e32 v4, v81, v4
	v_add_f32_e32 v5, v80, v5
	v_mfma_f32_32x32x16_bf16 v[114:129], v[198:201], v[146:149], v[114:129]
	ds_read_b64_tr_b16 v[210:211], v3 offset:51200
	ds_read_b64_tr_b16 v[212:213], v3 offset:51712
	v_add_f32_e32 v4, v51, v4
	v_add_f32_e32 v5, v50, v5
	v_add_f32_e32 v4, v53, v4
	v_add_f32_e32 v5, v52, v5
	v_mfma_f32_32x32x16_bf16 v[98:113], v[182:185], v[146:149], v[98:113]
	ds_read_b64_tr_b16 v[12:13], v3 offset:55296
	ds_read_b64_tr_b16 v[14:15], v3 offset:55808
	v_add_f32_e32 v4, v55, v4
	v_add_f32_e32 v5, v54, v5
	v_add_f32_e32 v4, v57, v4
	v_add_f32_e32 v5, v56, v5
	v_mfma_f32_32x32x16_bf16 v[114:129], v[190:193], v[150:153], v[114:129]
	ds_read_b64_tr_b16 v[8:9], v3 offset:52224
	ds_read_b64_tr_b16 v[10:11], v3 offset:52736
	v_add_f32_e32 v4, v59, v4
	v_add_f32_e32 v16, v61, v4
	v_add_f32_e32 v4, v58, v5
	v_add_f32_e32 v17, v60, v4
	v_mfma_f32_32x32x16_bf16 v[98:113], v[170:173], v[150:153], v[98:113]
	s_add_u32 s46, s46, s62
	s_addc_u32 s47, s47, s63
	s_and_b32 s64, s26, 3
	ds_read_b64_tr_b16 v[4:5], v3 offset:56320
	ds_read_b64_tr_b16 v[6:7], v3 offset:56832
	v_add_f32_e32 v3, v63, v16
	v_add_f32_e32 v16, v62, v17
	v_add_f32_e32 v3, v65, v3
	v_add_f32_e32 v16, v64, v16
	v_mfma_f32_32x32x16_bf16 v[114:129], v[178:181], v[154:157], v[114:129]
	s_mulk_i32 s64, 0x3000
	s_add_u32 s60, s60, 0x2000
	s_addc_u32 s61, s61, 0
	v_cvt_pk_bf16_f32 v178, v50, v51
	v_cvt_pk_bf16_f32 v179, v52, v53
	v_cvt_pk_bf16_f32 v186, v66, v67
	v_cvt_pk_bf16_f32 v187, v68, v69
	v_mfma_f32_32x32x16_bf16 v[98:113], v[166:169], v[154:157], v[98:113]
	s_add_i32 s52, s64, s91
	s_add_i32 s64, s42, 0x6000
	s_add_u32 s98, s98, s62
	s_addc_u32 s99, s99, s63
	v_cvt_pk_bf16_f32 v180, v54, v55
	v_cvt_pk_bf16_f32 v181, v56, v57
	v_cvt_pk_bf16_f32 v188, v70, v71
	v_cvt_pk_bf16_f32 v189, v72, v73
	v_mfma_f32_32x32x16_bf16 v[114:129], v[174:177], v[158:161], v[114:129]
	s_and_b32 s64, s64, 0x6000
	s_add_i32 s53, s64, s93
	v_cvt_pk_bf16_f32 v218, v58, v59
	v_cvt_pk_bf16_f32 v219, v60, v61
	v_cvt_pk_bf16_f32 v182, v74, v75
	v_cvt_pk_bf16_f32 v183, v76, v77
	v_mfma_f32_32x32x16_bf16 v[98:113], v[162:165], v[158:161], v[98:113]
	v_cvt_pk_bf16_f32 v220, v62, v63
	v_cvt_pk_bf16_f32 v221, v64, v65
	v_cvt_pk_bf16_f32 v184, v78, v79
	v_cvt_pk_bf16_f32 v185, v80, v81
	v_add_f32_e32 v3, v3, v16
	v_add_f32_e32 v246, v246, v3
	s_waitcnt lgkmcnt(0)
	v_mfma_f32_32x32x16_bf16 v[18:33], v[186:189], v[206:209], v[18:33]
	s_add_i32 s27, s26, 1
	s_and_b32 s64, s27, 3
	s_mulk_i32 s64, 0x3000
	v_exp_f32_e32 v66, v114
	v_exp_f32_e32 v67, v115
	v_exp_f32_e32 v68, v116
	v_exp_f32_e32 v69, v117
	v_add_u32_e32 v3, s64, v248
	v_mfma_f32_32x32x16_bf16 v[34:49], v[186:189], v[194:197], v[34:49]
	v_exp_f32_e32 v70, v118
	v_exp_f32_e32 v71, v119
	v_exp_f32_e32 v72, v120
	v_exp_f32_e32 v73, v121
	ds_read_b128 v[206:209], v3
	ds_read_b128 v[194:197], v3 offset:512
	v_mfma_f32_32x32x16_bf16 v[18:33], v[182:185], v[202:205], v[18:33]
	v_exp_f32_e32 v74, v122
	v_exp_f32_e32 v75, v123
	v_exp_f32_e32 v76, v124
	v_exp_f32_e32 v77, v125
	ds_read_b128 v[202:205], v3 offset:2048
	ds_read_b128 v[186:189], v3 offset:2560
	v_mfma_f32_32x32x16_bf16 v[34:49], v[182:185], v[214:217], v[34:49]
	v_exp_f32_e32 v78, v126
	v_exp_f32_e32 v79, v127
	v_exp_f32_e32 v80, v128
	v_exp_f32_e32 v81, v129
	ds_read_b128 v[198:201], v3 offset:4096
	ds_read_b128 v[182:185], v3 offset:4608
	v_mfma_f32_32x32x16_bf16 v[18:33], v[178:181], v[210:213], v[18:33]
	v_exp_f32_e32 v50, v98
	v_exp_f32_e32 v51, v99
	v_exp_f32_e32 v52, v100
	v_exp_f32_e32 v53, v101
	ds_read_b128 v[190:193], v3 offset:6144
	ds_read_b128 v[170:173], v3 offset:6656
	v_mfma_f32_32x32x16_bf16 v[34:49], v[178:181], v[12:15], v[34:49]
	v_exp_f32_e32 v54, v102
	v_exp_f32_e32 v55, v103
	v_exp_f32_e32 v56, v104
	v_exp_f32_e32 v57, v105
	ds_read_b128 v[178:181], v3 offset:8192
	ds_read_b128 v[166:169], v3 offset:8704
	v_mfma_f32_32x32x16_bf16 v[18:33], v[218:221], v[8:11], v[18:33]
	v_exp_f32_e32 v58, v106
	v_exp_f32_e32 v59, v107
	v_exp_f32_e32 v60, v108
	v_exp_f32_e32 v61, v109
	ds_read_b128 v[174:177], v3 offset:10240
	ds_read_b128 v[162:165], v3 offset:10752
	v_mfma_f32_32x32x16_bf16 v[34:49], v[218:221], v[4:7], v[34:49]
	v_exp_f32_e32 v62, v110
	v_exp_f32_e32 v63, v111
	v_exp_f32_e32 v64, v112
	v_exp_f32_e32 v65, v113
	s_mov_b32 s26, s27
	s_cmp_eq_u32 s27, s96
	s_cbranch_scc1 .Lmla_ss1_xdone
	s_add_i32 s64, s27, 3
	s_cmp_lt_u32 s64, s94
	s_cbranch_scc1 .Lmla_ss1_top
	s_waitcnt vmcnt(4)
	s_barrier
	s_branch .Lmla_ss_back
